# speedup vs baseline: 1.0021x; 1.0021x over previous
.LBB2_36:
	s_or_b64 exec, exec, s[12:13]
	v_mbcnt_lo_u32_b32 v5, -1, 0
	v_mbcnt_hi_u32_b32 v5, -1, v5
	v_and_b32_e32 v6, 64, v5
	v_add_u32_e32 v7, -1, v5
	v_cmp_lt_i32_e64 s[12:13], v7, v6
	v_and_b32_e32 v11, 63, v0
	v_add_u32_e32 v12, -2, v5
	v_cndmask_b32_e64 v7, v7, v5, s[12:13]
	v_lshlrev_b32_e32 v7, 2, v7
	ds_bpermute_b32 v7, v7, v10
	v_cmp_ne_u32_e64 s[12:13], 0, v11
	s_load_dwordx2 s[20:21], s[0:1], 0x18
	s_waitcnt lgkmcnt(0)
	v_cndmask_b32_e64 v7, 0, v7, s[12:13]
	v_cmp_lt_i32_e64 s[12:13], v12, v6
	v_add_u32_e32 v7, v7, v10
	s_nop 0
	v_cndmask_b32_e64 v12, v12, v5, s[12:13]
	v_lshlrev_b32_e32 v12, 2, v12
	ds_bpermute_b32 v12, v12, v7
	v_cmp_lt_u32_e64 s[12:13], 1, v11
	s_waitcnt lgkmcnt(0)
	s_nop 0
	v_cndmask_b32_e64 v12, 0, v12, s[12:13]
	v_add_u32_e32 v7, v12, v7
	v_add_u32_e32 v12, -4, v5
	v_cmp_lt_i32_e64 s[12:13], v12, v6
	s_nop 1
	v_cndmask_b32_e64 v12, v12, v5, s[12:13]
	v_lshlrev_b32_e32 v12, 2, v12
	ds_bpermute_b32 v12, v12, v7
	v_cmp_lt_u32_e64 s[12:13], 3, v11
	s_waitcnt lgkmcnt(0)
	s_nop 0
	v_cndmask_b32_e64 v12, 0, v12, s[12:13]
	v_add_u32_e32 v7, v12, v7
	v_add_u32_e32 v12, -8, v5
	v_cmp_lt_i32_e64 s[12:13], v12, v6
	s_nop 1
	v_cndmask_b32_e64 v12, v12, v5, s[12:13]
	v_lshlrev_b32_e32 v12, 2, v12
	ds_bpermute_b32 v12, v12, v7
	v_cmp_lt_u32_e64 s[12:13], 7, v11
	s_waitcnt lgkmcnt(0)
	s_nop 0
	v_cndmask_b32_e64 v12, 0, v12, s[12:13]
	v_add_u32_e32 v7, v12, v7
	v_add_u32_e32 v12, -16, v5
	v_cmp_lt_i32_e64 s[12:13], v12, v6
	s_nop 1
	v_cndmask_b32_e64 v12, v12, v5, s[12:13]
	v_lshlrev_b32_e32 v12, 2, v12
	ds_bpermute_b32 v12, v12, v7
	v_cmp_lt_u32_e64 s[12:13], 15, v11
	s_waitcnt lgkmcnt(0)
	s_nop 0
	v_cndmask_b32_e64 v12, 0, v12, s[12:13]
	v_add_u32_e32 v12, v12, v7
	v_subrev_u32_e32 v7, 32, v5
	v_cmp_lt_i32_e64 s[12:13], v7, v6
	s_nop 1
	v_cndmask_b32_e64 v5, v7, v5, s[12:13]
	v_lshlrev_b32_e32 v5, 2, v5
	ds_bpermute_b32 v5, v5, v12
	v_cmp_lt_u32_e64 s[12:13], 31, v11
	v_lshrrev_b32_e32 v7, 6, v0
	s_waitcnt lgkmcnt(0)
	v_cndmask_b32_e64 v5, 0, v5, s[12:13]
	v_add_u32_e32 v6, v5, v12
	v_cmp_eq_u32_e64 s[12:13], 63, v11
	s_and_saveexec_b64 s[24:25], s[12:13]
	v_lshlrev_b32_e32 v5, 2, v7
	ds_write_b32 v5, v6 offset:5888
	s_or_b64 exec, exec, s[24:25]
	v_mov_b32_e32 v5, 0
	s_waitcnt lgkmcnt(0)
	s_barrier
	ds_read_b128 v[12:15], v5 offset:5888
	ds_read_b128 v[16:19], v5 offset:5904
	ds_read_b128 v[20:23], v5 offset:5920
	ds_read_b96 v[24:26], v5 offset:5936
	v_cmp_lt_u32_e64 s[12:13], 63, v0
	s_waitcnt lgkmcnt(0)
	s_barrier
	v_cndmask_b32_e64 v11, 0, v12, s[12:13]
	s_movk_i32 s12, 0x7f
	v_cmp_lt_u32_e64 s[12:13], s12, v0
	s_nop 1
	v_cndmask_b32_e64 v12, 0, v13, s[12:13]
	s_movk_i32 s12, 0xbf
	v_cmp_lt_u32_e64 s[12:13], s12, v0
	s_nop 1
	v_cndmask_b32_e64 v13, 0, v14, s[12:13]
	s_movk_i32 s12, 0xff
	v_cmp_lt_u32_e64 s[12:13], s12, v0
	s_nop 1
	v_cndmask_b32_e64 v14, 0, v15, s[12:13]
	s_movk_i32 s12, 0x13f
	v_cmp_lt_u32_e64 s[12:13], s12, v0
	s_nop 1
	v_cndmask_b32_e64 v15, 0, v16, s[12:13]
	s_movk_i32 s12, 0x17f
	v_cmp_lt_u32_e64 s[12:13], s12, v0
	s_nop 1
	v_cndmask_b32_e64 v16, 0, v17, s[12:13]
	s_movk_i32 s12, 0x1bf
	v_cmp_lt_u32_e64 s[12:13], s12, v0
	s_nop 1
	v_cndmask_b32_e64 v17, 0, v18, s[12:13]
	s_movk_i32 s12, 0x1ff
	v_cmp_lt_u32_e64 s[12:13], s12, v0
	s_nop 1
	v_cndmask_b32_e64 v18, 0, v19, s[12:13]
	s_movk_i32 s12, 0x23f
	v_cmp_lt_u32_e64 s[12:13], s12, v0
	s_nop 1
	v_cndmask_b32_e64 v19, 0, v20, s[12:13]
	s_movk_i32 s12, 0x27f
	v_cmp_lt_u32_e64 s[12:13], s12, v0
	s_nop 1
	v_cndmask_b32_e64 v20, 0, v21, s[12:13]
	s_movk_i32 s12, 0x2bf
	v_cmp_lt_u32_e64 s[12:13], s12, v0
	s_nop 1
	v_cndmask_b32_e64 v21, 0, v22, s[12:13]
	s_movk_i32 s12, 0x2ff
	v_cmp_lt_u32_e64 s[12:13], s12, v0
	s_nop 1
	v_cndmask_b32_e64 v22, 0, v23, s[12:13]
	s_movk_i32 s12, 0x33f
	v_cmp_lt_u32_e64 s[12:13], s12, v0
	s_nop 1
	v_cndmask_b32_e64 v23, 0, v24, s[12:13]
	s_movk_i32 s12, 0x37f
	v_cmp_lt_u32_e64 s[12:13], s12, v0
	s_nop 1
	v_cndmask_b32_e64 v24, 0, v25, s[12:13]
	v_cmp_eq_u32_e64 s[12:13], 15, v7
	s_nop 1
	v_cndmask_b32_e64 v7, 0, v26, s[12:13]
	s_add_i32 s12, s16, s26
	v_sub_u32_e32 v25, s12, v10
	v_add3_u32 v6, v25, v6, v11
	v_add3_u32 v6, v6, v12, v13
	v_add3_u32 v6, v6, v14, v15
	v_add3_u32 v6, v6, v16, v17
	v_add3_u32 v6, v6, v18, v19
	v_add3_u32 v6, v6, v20, v21
	v_add3_u32 v6, v6, v22, v23
	v_add3_u32 v6, v6, v24, v7
	s_add_i32 s44, s16, s26
	s_and_saveexec_b64 s[24:25], s[22:23]
	s_cbranch_execz .LBB2_41
	s_load_dwordx2 s[22:23], s[0:1], 0x10
	v_ashrrev_i32_e32 v7, 31, v6
	s_mov_b32 s12, 0x1869f
	v_lshl_add_u64 v[12:13], v[6:7], 2, s[20:21]
	s_sub_i32 s45, s17, s16
	s_cmpk_le_i32 s45, 0x1400
	s_cbranch_scc1 .Lc8_nost
	global_store_dword v[12:13], v4, off
.Lc8_nost:
	v_subrev_u32_e32 v28, s44, v6
	v_lshlrev_b32_e32 v28, 2, v28
	ds_write_b32 v28, v4 offset:38720
	s_waitcnt lgkmcnt(0)
	v_lshl_add_u64 v[12:13], v[4:5], 2, s[22:23]
	v_cmp_eq_u32_e64 s[12:13], s12, v4
	global_store_dword v[12:13], v6, off
	s_and_b64 exec, exec, s[12:13]
	s_cbranch_execz .LBB2_41
	v_add_u32_e32 v4, v6, v10
	v_mov_b32_e32 v5, 0x61000
	global_store_dword v5, v4, s[22:23] offset:2688
